# N2 + key-loop back edge rotated (closing barrier as loop head, exit path with its own barrier copy)
# baseline (speedup 1.0000x reference)
.LBB0_757:
	s_barrier
	ds_read_b128 v[64:67], v180 offset:49152
	ds_read_b128 v[68:71], v180 offset:57344
	ds_read_b128 v[200:203], v181 offset:49152
	ds_read_b128 v[226:229], v181 offset:57344
	ds_read_b128 v[230:233], v182 offset:49152
	ds_read_b128 v[234:237], v182 offset:57344
	ds_read_b128 v[238:241], v183 offset:49152
	ds_read_b128 v[242:245], v183 offset:57344
	s_add_i32 s6, 0, 0x12000
	v_add_u32_e32 v199, s6, v170
	v_add_u32_e32 v204, s6, v171
	v_add_u32_e32 v205, s6, v172
	s_waitcnt lgkmcnt(7)
	v_mfma_f32_32x32x16_bf16 v[80:95], v[64:67], v[124:127], 0
	s_add_i32 s12, s64, -1
	s_sub_i32 s80, s11, 64
	s_cmp_lt_u32 s12, 3
	s_cselect_b32 s80, s10, s80
	s_mul_i32 s81, s80, 0xc00
	s_add_i32 s85, s82, 0x8000
	s_mov_b32 m0, s85
	s_add_i32 s85, s82, 0x10000
	buffer_load_dwordx4 v154, s[72:75], s81 offen lds
	v_exp_f32_e32 v216, v128
	v_add_f32_e32 v128, 0, v222
	v_add_f32_e32 v128, v224, v128
	v_add_f32_e32 v128, v220, v128
	v_add_f32_e32 v128, v223, v128
	v_add_f32_e32 v128, v219, v128
	v_add_f32_e32 v128, v221, v128
	s_waitcnt lgkmcnt(6)
	v_mfma_f32_32x32x16_bf16 v[64:79], v[68:71], v[124:127], 0
	s_mov_b32 m0, s85
	s_add_i32 s85, s82, 0xa000
	buffer_load_dwordx4 v155, s[72:75], s81 offen lds
	v_add_f32_e32 v128, v217, v128
	v_add_f32_e32 v128, v218, v128
	v_add_f32_e32 v128, v212, v128
	v_add_f32_e32 v128, v214, v128
	v_add_f32_e32 v128, v211, v128
	v_add_f32_e32 v128, v213, v128
	v_exp_f32_e32 v138, v138
	s_waitcnt lgkmcnt(5)
	v_mfma_f32_32x32x16_bf16 v[80:95], v[200:203], v[120:123], v[80:95]
	s_mov_b32 m0, s85
	s_add_i32 s81, s81, 0x18000
	buffer_load_dwordx4 v154, s[72:75], s81 offen lds
	v_add_f32_e32 v128, v208, v128
	v_exp_f32_e32 v139, v139
	v_add_f32_e32 v128, v210, v128
	v_exp_f32_e32 v164, v136
	v_add_f32_e32 v128, v207, v128
	v_exp_f32_e32 v137, v137
	v_add_f32_e32 v128, v209, v128
	s_waitcnt lgkmcnt(4)
	v_mfma_f32_32x32x16_bf16 v[64:79], v[226:229], v[120:123], v[64:79]
	s_lshl_b32 s81, s83, 11
	s_add_i32 s85, s82, 0x4000
	s_mov_b32 m0, s85
	s_add_i32 s85, s82, 0x6000
	buffer_load_dwordx4 v158, s[76:79], s81 offen lds
	ds_read_b128 v[200:203], v184 offset:49152
	ds_read_b128 v[226:229], v184 offset:57344
	v_exp_f32_e32 v165, v132
	v_add_f32_e32 v128, v138, v128
	v_add_f32_e32 v128, v139, v128
	v_exp_f32_e32 v206, v130
	v_add_f32_e32 v128, v164, v128
	v_exp_f32_e32 v215, v131
	s_waitcnt lgkmcnt(5)
	v_mfma_f32_32x32x16_bf16 v[80:95], v[230:233], v[116:119], v[80:95]
	s_mov_b32 m0, s85
	s_add_i32 s81, s81, 0x10000
	buffer_load_dwordx4 v158, s[76:79], s81 offen lds
	s_mov_b32 s84, s80
	v_add_f32_e32 v128, v137, v128
	v_add_f32_e32 v128, v165, v128
	v_exp_f32_e32 v225, v129
	v_exp_f32_e32 v162, v162
	v_exp_f32_e32 v163, v163
	v_exp_f32_e32 v160, v160
	v_exp_f32_e32 v161, v161
	s_waitcnt lgkmcnt(4)
	v_mfma_f32_32x32x16_bf16 v[64:79], v[234:237], v[116:119], v[64:79]
	ds_read_b128 v[230:233], v185 offset:49152
	ds_read_b128 v[234:237], v185 offset:57344
	v_cvt_pk_bf16_f32 v129, v220, v223
	v_cvt_pk_bf16_f32 v130, v219, v221
	v_cvt_pk_bf16_f32 v131, v217, v218
	v_cvt_pk_bf16_f32 v132, v212, v214
	v_cvt_pk_bf16_f32 v136, v138, v139
	v_cvt_pk_bf16_f32 v137, v164, v137
	s_waitcnt lgkmcnt(5)
	v_mfma_f32_32x32x16_bf16 v[80:95], v[238:241], v[112:115], v[80:95]
	v_cvt_pk_bf16_f32 v139, v206, v215
	v_permlane32_swap_b32_e32 v129, v131
	s_nop 0
	v_permlane32_swap_b32_e32 v137, v139
	s_waitcnt lgkmcnt(4)
	v_mfma_f32_32x32x16_bf16 v[64:79], v[242:245], v[112:115], v[64:79]
	ds_read_b128 v[238:241], v186 offset:49152
	ds_read_b128 v[242:245], v186 offset:57344
	s_waitcnt lgkmcnt(5)
	v_mfma_f32_32x32x16_bf16 v[80:95], v[200:203], v[108:111], v[80:95]
	s_waitcnt lgkmcnt(4)
	v_mfma_f32_32x32x16_bf16 v[64:79], v[226:229], v[108:111], v[64:79]
	ds_read_b128 v[200:203], v187 offset:49152
	ds_read_b128 v[226:229], v187 offset:57344
	s_waitcnt lgkmcnt(5)
	v_mfma_f32_32x32x16_bf16 v[80:95], v[230:233], v[104:107], v[80:95]
	s_waitcnt lgkmcnt(4)
	v_mfma_f32_32x32x16_bf16 v[64:79], v[234:237], v[104:107], v[64:79]
	ds_read_b128 v[230:233], v199
	ds_read_b128 v[234:237], v199 offset:4096
	ds_read_b128 v[246:249], v190
	s_waitcnt lgkmcnt(6)
	v_mfma_f32_32x32x16_bf16 v[80:95], v[238:241], v[100:103], v[80:95]
	s_waitcnt lgkmcnt(5)
	v_mfma_f32_32x32x16_bf16 v[64:79], v[242:245], v[100:103], v[64:79]
	ds_read_b128 v[238:241], v204
	ds_read_b128 v[242:245], v204 offset:4096
	ds_read_b128 v[250:253], v190 offset:1024
	v_add_u32_e32 v204, s6, v173
	s_waitcnt lgkmcnt(7)
	v_mfma_f32_32x32x16_bf16 v[80:95], v[200:203], v[96:99], v[80:95]
	s_waitcnt lgkmcnt(6)
	v_mfma_f32_32x32x16_bf16 v[64:79], v[226:229], v[96:99], v[64:79]
	ds_read_b128 v[200:203], v205
	ds_read_b128 v[226:229], v205 offset:4096
	s_waitcnt lgkmcnt(5)
	v_mfma_f32_32x32x16_bf16 v[80:95], v[230:233], v[246:249], v[80:95]
	s_waitcnt lgkmcnt(5)
	v_mfma_f32_32x32x16_bf16 v[64:79], v[234:237], v[246:249], v[64:79]
	ds_read_b128 v[230:233], v204
	ds_read_b128 v[234:237], v204 offset:4096
	ds_read_b128 v[246:249], v190 offset:2048
	s_waitcnt lgkmcnt(5)
	v_mfma_f32_32x32x16_bf16 v[80:95], v[238:241], v[250:253], v[80:95]
	s_waitcnt lgkmcnt(5)
	v_mfma_f32_32x32x16_bf16 v[64:79], v[242:245], v[250:253], v[64:79]
	ds_read_b128 v[250:253], v190 offset:3072
	s_waitcnt lgkmcnt(1)
	v_mfma_f32_32x32x16_bf16 v[80:95], v[200:203], v[246:249], v[80:95]
	v_exp_f32_e32 v205, v133
	v_cvt_pk_bf16_f32 v133, v211, v213
	v_cvt_pk_bf16_f32 v138, v165, v205
	v_add_f32_e32 v128, v205, v128
	v_add_f32_e32 v128, v206, v128
	v_add_f32_e32 v128, v215, v128
	s_waitcnt lgkmcnt(1)
	v_mfma_f32_32x32x16_bf16 v[64:79], v[226:229], v[246:249], v[64:79]
	v_add_f32_e32 v128, v216, v128
	v_add_f32_e32 v128, v225, v128
	v_add_f32_e32 v128, v162, v128
	v_add_f32_e32 v128, v163, v128
	v_add_f32_e32 v128, v160, v128
	v_add_f32_e32 v128, v161, v128
	s_waitcnt lgkmcnt(0)
	v_mfma_f32_32x32x16_bf16 v[80:95], v[230:233], v[250:253], v[80:95]
	v_exp_f32_e32 v226, v134
	v_exp_f32_e32 v227, v135
	v_cvt_pk_bf16_f32 v134, v208, v210
	v_cvt_pk_bf16_f32 v135, v207, v209
	v_add_f32_e32 v128, v226, v128
	v_add_f32_e32 v203, v227, v128
	v_mov_b32_e32 v204, v203
	s_waitcnt lgkmcnt(0)
	v_mfma_f32_32x32x16_bf16 v[64:79], v[234:237], v[250:253], v[64:79]
	s_nop 0
	v_permlane32_swap_b32_e32 v203, v204
	v_cvt_pk_bf16_f32 v128, v222, v224
	v_cvt_pk_bf16_f32 v208, v216, v225
	v_cvt_pk_bf16_f32 v209, v162, v163
	v_cvt_pk_bf16_f32 v210, v160, v161
	v_cvt_pk_bf16_f32 v211, v226, v227
	v_permlane32_swap_b32_e32 v132, v134
	v_permlane32_swap_b32_e32 v128, v130
	v_permlane32_swap_b32_e32 v133, v135
	v_permlane32_swap_b32_e32 v136, v138
	v_permlane32_swap_b32_e32 v208, v210
	v_permlane32_swap_b32_e32 v209, v211
	ds_read_b64_tr_b16 v[160:161], v167 offset:0
	ds_read_b64_tr_b16 v[162:163], v167 offset:0x800
	ds_read_b64_tr_b16 v[232:233], v167 offset:0x1000
	ds_read_b64_tr_b16 v[234:235], v167 offset:0x1800
	ds_read_b64_tr_b16 v[236:237], v167 offset:0x2000
	ds_read_b64_tr_b16 v[238:239], v167 offset:0x2800
	ds_read_b64_tr_b16 v[240:241], v167 offset:0x3000
	ds_read_b64_tr_b16 v[242:243], v167 offset:0x3800
	v_max_f32_e32 v164, v81, v81
	v_max_f32_e32 v165, v80, v80
	v_max_f32_e32 v164, v165, v164
	v_max3_f32 v164, v164, v82, v83
	v_max3_f32 v164, v164, v84, v85
	v_max3_f32 v164, v164, v86, v87
	v_max3_f32 v164, v164, v88, v89
	v_max3_f32 v164, v164, v90, v91
	v_max3_f32 v164, v164, v92, v93
	v_max3_f32 v164, v164, v94, v95
	s_waitcnt lgkmcnt(0)
	v_mfma_f32_32x32x16_bf16 v[16:31], v[128:131], v[160:163], v[16:31]
	v_max3_f32 v160, v164, v64, v65
	v_max3_f32 v160, v160, v66, v67
	v_max3_f32 v160, v160, v68, v69
	v_mfma_f32_32x32x16_bf16 v[16:31], v[132:135], v[232:235], v[16:31]
	ds_read_b64_tr_b16 v[232:233], v167 offset:0x200
	ds_read_b64_tr_b16 v[234:235], v167 offset:0xa00
	v_max3_f32 v160, v160, v70, v71
	v_max3_f32 v160, v160, v72, v73
	v_max3_f32 v160, v160, v74, v75
	v_mfma_f32_32x32x16_bf16 v[16:31], v[136:139], v[236:239], v[16:31]
	ds_read_b64_tr_b16 v[236:237], v167 offset:0x1200
	ds_read_b64_tr_b16 v[238:239], v167 offset:0x1a00
	ds_read_b64_tr_b16 v[244:245], v167 offset:0x2200
	ds_read_b64_tr_b16 v[246:247], v167 offset:0x2a00
	ds_read_b64_tr_b16 v[248:249], v167 offset:0x3200
	ds_read_b64_tr_b16 v[250:251], v167 offset:0x3a00
	v_max3_f32 v160, v160, v76, v77
	v_max3_f32 v160, v160, v78, v79
	v_mov_b32_e32 v161, v160
	v_mfma_f32_32x32x16_bf16 v[16:31], v[208:211], v[240:243], v[16:31]
	v_max_f32_e32 v162, v198, v198
	v_permlane32_swap_b32_e32 v160, v161
	v_max_f32_e32 v161, v161, v161
	v_max_f32_e32 v160, v160, v160
	v_max_f32_e32 v160, v160, v161
	s_waitcnt lgkmcnt(0)
	v_mfma_f32_32x32x16_bf16 v[32:47], v[128:131], v[232:235], v[32:47]
	ds_read_b64_tr_b16 v[232:233], v167 offset:0x400
	ds_read_b64_tr_b16 v[234:235], v167 offset:0xc00
	v_sub_f32_e32 v161, v160, v198
	v_max_f32_e32 v160, v162, v160
	v_sub_f32_e32 v162, v198, v160
	v_mul_f32_e32 v162, 0x3dd53b94, v162
	v_exp_f32_e32 v162, v162
	v_mfma_f32_32x32x16_bf16 v[32:47], v[132:135], v[236:239], v[32:47]
	ds_read_b64_tr_b16 v[236:237], v167 offset:0x1400
	ds_read_b64_tr_b16 v[238:239], v167 offset:0x1c00
	ds_read_b64_tr_b16 v[240:241], v167 offset:0x2400
	ds_read_b64_tr_b16 v[242:243], v167 offset:0x2c00
	v_cmp_ge_f32_e32 vcc, s48, v161
	s_cmp_eq_u64 vcc, exec
	s_cselect_b64 s[6:7], -1, 0
	v_cndmask_b32_e64 v206, v162, 1.0, s[6:7]
	v_cndmask_b32_e64 v160, v160, v198, s[6:7]
	v_mul_f32_e32 v205, 0xbdd53b94, v160
	v_cmp_gt_f32_e32 vcc, 1.0, v206
	v_mfma_f32_32x32x16_bf16 v[32:47], v[136:139], v[244:247], v[32:47]
	ds_read_b64_tr_b16 v[244:245], v167 offset:0x3400
	ds_read_b64_tr_b16 v[246:247], v167 offset:0x3c00
	v_fmamk_f32 v87, v87, 0x3dd53b94, v205
	v_fmamk_f32 v80, v80, 0x3dd53b94, v205
	v_fmamk_f32 v81, v81, 0x3dd53b94, v205
	v_fmamk_f32 v82, v82, 0x3dd53b94, v205
	v_fmamk_f32 v83, v83, 0x3dd53b94, v205
	v_mfma_f32_32x32x16_bf16 v[32:47], v[208:211], v[248:251], v[32:47]
	v_fmamk_f32 v84, v84, 0x3dd53b94, v205
	v_fmamk_f32 v85, v85, 0x3dd53b94, v205
	v_fmamk_f32 v86, v86, 0x3dd53b94, v205
	v_fmamk_f32 v88, v88, 0x3dd53b94, v205
	v_fmamk_f32 v89, v89, 0x3dd53b94, v205
	s_waitcnt lgkmcnt(0)
	v_mfma_f32_32x32x16_bf16 v[0:15], v[128:131], v[232:235], v[0:15]
	ds_read_b64_tr_b16 v[232:233], v167 offset:0x600
	ds_read_b64_tr_b16 v[234:235], v167 offset:0xe00
	v_fmamk_f32 v90, v90, 0x3dd53b94, v205
	v_fmamk_f32 v91, v91, 0x3dd53b94, v205
	v_fmamk_f32 v92, v92, 0x3dd53b94, v205
	v_fmamk_f32 v93, v93, 0x3dd53b94, v205
	v_fmamk_f32 v94, v94, 0x3dd53b94, v205
	v_mfma_f32_32x32x16_bf16 v[0:15], v[132:135], v[236:239], v[0:15]
	ds_read_b64_tr_b16 v[236:237], v167 offset:0x1600
	ds_read_b64_tr_b16 v[238:239], v167 offset:0x1e00
	v_fmamk_f32 v95, v95, 0x3dd53b94, v205
	v_fmamk_f32 v215, v64, 0x3dd53b94, v205
	v_fmamk_f32 v216, v65, 0x3dd53b94, v205
	v_fmamk_f32 v217, v66, 0x3dd53b94, v205
	v_fmamk_f32 v218, v67, 0x3dd53b94, v205
	v_mfma_f32_32x32x16_bf16 v[0:15], v[136:139], v[240:243], v[0:15]
	ds_read_b64_tr_b16 v[240:241], v167 offset:0x2600
	ds_read_b64_tr_b16 v[242:243], v167 offset:0x2e00
	ds_read_b64_tr_b16 v[248:249], v167 offset:0x3600
	ds_read_b64_tr_b16 v[250:251], v167 offset:0x3e00
	v_fmamk_f32 v219, v68, 0x3dd53b94, v205
	v_fmamk_f32 v212, v73, 0x3dd53b94, v205
	v_fmamk_f32 v213, v74, 0x3dd53b94, v205
	v_fmamk_f32 v214, v75, 0x3dd53b94, v205
	v_mfma_f32_32x32x16_bf16 v[0:15], v[208:211], v[244:247], v[0:15]
	v_fmamk_f32 v207, v76, 0x3dd53b94, v205
	v_fmamk_f32 v220, v77, 0x3dd53b94, v205
	v_fmamk_f32 v221, v78, 0x3dd53b94, v205
	s_waitcnt lgkmcnt(0)
	v_mfma_f32_32x32x16_bf16 v[48:63], v[128:131], v[232:235], v[48:63]
	v_exp_f32_e32 v128, v80
	v_exp_f32_e32 v129, v82
	v_exp_f32_e32 v130, v84
	v_exp_f32_e32 v131, v86
	v_mfma_f32_32x32x16_bf16 v[48:63], v[132:135], v[236:239], v[48:63]
	v_exp_f32_e32 v132, v88
	v_exp_f32_e32 v133, v90
	v_exp_f32_e32 v134, v92
	v_exp_f32_e32 v135, v94
	v_mfma_f32_32x32x16_bf16 v[48:63], v[136:139], v[240:243], v[48:63]
	v_exp_f32_e32 v139, v89
	v_exp_f32_e32 v138, v91
	v_exp_f32_e32 v137, v93
	v_exp_f32_e32 v136, v95
	v_mfma_f32_32x32x16_bf16 v[48:63], v[208:211], v[248:251], v[48:63]
	v_exp_f32_e32 v161, v87
	v_exp_f32_e32 v198, v81
	v_exp_f32_e32 v163, v83
	v_exp_f32_e32 v162, v85
	v_fmamk_f32 v208, v69, 0x3dd53b94, v205
	v_fmamk_f32 v209, v70, 0x3dd53b94, v205
	v_fmamk_f32 v210, v71, 0x3dd53b94, v205
	v_fmamk_f32 v211, v72, 0x3dd53b94, v205
	v_fmac_f32_e32 v205, 0x3dd53b94, v79
	s_cbranch_vccz .LBB0_761
	s_and_saveexec_b64 s[8:9], s[4:5]
	ds_write_b32 v189, v206 offset:128
	s_or_b64 exec, exec, s[8:9]
	s_waitcnt lgkmcnt(0)
	v_add_u32_e32 v248, s62, v169
	ds_read_b128 v[232:235], v248 offset:224
	ds_read_b128 v[236:239], v248 offset:192
	ds_read_b128 v[240:243], v248 offset:160
	ds_read_b128 v[244:247], v248 offset:128
	s_waitcnt lgkmcnt(3)
	v_pk_mul_f32 v[28:29], v[28:29], v[232:233]
	s_waitcnt lgkmcnt(2)
	v_pk_mul_f32 v[24:25], v[24:25], v[236:237]
	s_waitcnt lgkmcnt(1)
	v_pk_mul_f32 v[20:21], v[20:21], v[240:241]
	v_pk_mul_f32 v[30:31], v[30:31], v[234:235]
	v_pk_mul_f32 v[26:27], v[26:27], v[238:239]
	v_pk_mul_f32 v[22:23], v[22:23], v[242:243]
	s_waitcnt lgkmcnt(0)
	v_pk_mul_f32 v[18:19], v[18:19], v[246:247]
	v_pk_mul_f32 v[16:17], v[16:17], v[244:245]
	v_pk_mul_f32 v[44:45], v[44:45], v[232:233]
	v_pk_mul_f32 v[40:41], v[40:41], v[236:237]
	v_pk_mul_f32 v[36:37], v[36:37], v[240:241]
	v_pk_mul_f32 v[46:47], v[46:47], v[234:235]
	v_pk_mul_f32 v[42:43], v[42:43], v[238:239]
	v_pk_mul_f32 v[38:39], v[38:39], v[242:243]
	v_pk_mul_f32 v[34:35], v[34:35], v[246:247]
	v_pk_mul_f32 v[32:33], v[32:33], v[244:245]
	v_pk_mul_f32 v[12:13], v[12:13], v[232:233]
	v_pk_mul_f32 v[8:9], v[8:9], v[236:237]
	v_pk_mul_f32 v[4:5], v[4:5], v[240:241]
	v_pk_mul_f32 v[14:15], v[14:15], v[234:235]
	v_pk_mul_f32 v[10:11], v[10:11], v[238:239]
	v_pk_mul_f32 v[6:7], v[6:7], v[242:243]
	v_pk_mul_f32 v[2:3], v[2:3], v[246:247]
	v_pk_mul_f32 v[0:1], v[0:1], v[244:245]
	v_pk_mul_f32 v[60:61], v[60:61], v[232:233]
	v_pk_mul_f32 v[56:57], v[56:57], v[236:237]
	v_pk_mul_f32 v[52:53], v[52:53], v[240:241]
	v_pk_mul_f32 v[62:63], v[62:63], v[234:235]
	v_pk_mul_f32 v[58:59], v[58:59], v[238:239]
	v_pk_mul_f32 v[54:55], v[54:55], v[242:243]
	v_pk_mul_f32 v[50:51], v[50:51], v[246:247]
	v_pk_mul_f32 v[48:49], v[48:49], v[244:245]

.LBB0_2012:
	s_barrier
	ds_read_b128 v[64:67], v180 offset:49152
	ds_read_b128 v[68:71], v180 offset:57344
	ds_read_b128 v[200:203], v181 offset:49152
	ds_read_b128 v[226:229], v181 offset:57344
	ds_read_b128 v[230:233], v182 offset:49152
	ds_read_b128 v[234:237], v182 offset:57344
	ds_read_b128 v[238:241], v183 offset:49152
	ds_read_b128 v[242:245], v183 offset:57344
	s_add_i32 s6, 0, 0x12000
	v_add_u32_e32 v199, s6, v170
	v_add_u32_e32 v204, s6, v171
	v_add_u32_e32 v205, s6, v172
	s_waitcnt lgkmcnt(7)
	v_mfma_f32_32x32x16_bf16 v[80:95], v[64:67], v[124:127], 0
	s_add_i32 s8, s8, 2
	s_sub_i32 s80, s14, 64
	s_cmp_lt_u32 s8, 3
	s_cselect_b32 s80, s13, s80
	s_mul_i32 s81, s80, 0xc00
	s_add_i32 s85, s82, 0x8000
	s_mov_b32 m0, s85
	s_add_i32 s85, s82, 0x10000
	buffer_load_dwordx4 v154, s[72:75], s81 offen lds
	v_exp_f32_e32 v216, v128
	v_add_f32_e32 v128, 0, v222
	v_add_f32_e32 v128, v224, v128
	v_add_f32_e32 v128, v220, v128
	v_add_f32_e32 v128, v223, v128
	v_add_f32_e32 v128, v219, v128
	v_add_f32_e32 v128, v221, v128
	s_waitcnt lgkmcnt(6)
	v_mfma_f32_32x32x16_bf16 v[64:79], v[68:71], v[124:127], 0
	s_mov_b32 m0, s85
	s_add_i32 s85, s82, 0xa000
	buffer_load_dwordx4 v155, s[72:75], s81 offen lds
	v_add_f32_e32 v128, v217, v128
	v_add_f32_e32 v128, v218, v128
	v_add_f32_e32 v128, v212, v128
	v_add_f32_e32 v128, v214, v128
	v_add_f32_e32 v128, v211, v128
	v_add_f32_e32 v128, v213, v128
	v_exp_f32_e32 v138, v138
	s_waitcnt lgkmcnt(5)
	v_mfma_f32_32x32x16_bf16 v[80:95], v[200:203], v[120:123], v[80:95]
	s_mov_b32 m0, s85
	s_add_i32 s81, s81, 0x18000
	buffer_load_dwordx4 v154, s[72:75], s81 offen lds
	v_add_f32_e32 v128, v208, v128
	v_exp_f32_e32 v139, v139
	v_add_f32_e32 v128, v210, v128
	v_exp_f32_e32 v164, v136
	v_add_f32_e32 v128, v207, v128
	v_exp_f32_e32 v137, v137
	v_add_f32_e32 v128, v209, v128
	s_waitcnt lgkmcnt(4)
	v_mfma_f32_32x32x16_bf16 v[64:79], v[226:229], v[120:123], v[64:79]
	s_lshl_b32 s81, s83, 11
	s_add_i32 s85, s82, 0x4000
	s_mov_b32 m0, s85
	s_add_i32 s85, s82, 0x6000
	buffer_load_dwordx4 v158, s[76:79], s81 offen lds
	ds_read_b128 v[200:203], v184 offset:49152
	ds_read_b128 v[226:229], v184 offset:57344
	v_exp_f32_e32 v165, v132
	v_add_f32_e32 v128, v138, v128
	v_add_f32_e32 v128, v139, v128
	v_exp_f32_e32 v206, v130
	v_add_f32_e32 v128, v164, v128
	v_exp_f32_e32 v215, v131
	s_waitcnt lgkmcnt(5)
	v_mfma_f32_32x32x16_bf16 v[80:95], v[230:233], v[116:119], v[80:95]
	s_mov_b32 m0, s85
	s_add_i32 s81, s81, 0x10000
	buffer_load_dwordx4 v158, s[76:79], s81 offen lds
	s_mov_b32 s84, s80
	v_add_f32_e32 v128, v137, v128
	v_add_f32_e32 v128, v165, v128
	v_exp_f32_e32 v225, v129
	v_exp_f32_e32 v162, v162
	v_exp_f32_e32 v163, v163
	v_exp_f32_e32 v160, v160
	v_exp_f32_e32 v161, v161
	s_waitcnt lgkmcnt(4)
	v_mfma_f32_32x32x16_bf16 v[64:79], v[234:237], v[116:119], v[64:79]
	ds_read_b128 v[230:233], v185 offset:49152
	ds_read_b128 v[234:237], v185 offset:57344
	v_cvt_pk_bf16_f32 v129, v220, v223
	v_cvt_pk_bf16_f32 v130, v219, v221
	v_cvt_pk_bf16_f32 v131, v217, v218
	v_cvt_pk_bf16_f32 v132, v212, v214
	v_cvt_pk_bf16_f32 v136, v138, v139
	v_cvt_pk_bf16_f32 v137, v164, v137
	s_waitcnt lgkmcnt(5)
	v_mfma_f32_32x32x16_bf16 v[80:95], v[238:241], v[112:115], v[80:95]
	v_cvt_pk_bf16_f32 v139, v206, v215
	v_permlane32_swap_b32_e32 v129, v131
	s_nop 0
	v_permlane32_swap_b32_e32 v137, v139
	s_waitcnt lgkmcnt(4)
	v_mfma_f32_32x32x16_bf16 v[64:79], v[242:245], v[112:115], v[64:79]
	ds_read_b128 v[238:241], v186 offset:49152
	ds_read_b128 v[242:245], v186 offset:57344
	s_waitcnt lgkmcnt(5)
	v_mfma_f32_32x32x16_bf16 v[80:95], v[200:203], v[108:111], v[80:95]
	s_waitcnt lgkmcnt(4)
	v_mfma_f32_32x32x16_bf16 v[64:79], v[226:229], v[108:111], v[64:79]
	ds_read_b128 v[200:203], v187 offset:49152
	ds_read_b128 v[226:229], v187 offset:57344
	s_waitcnt lgkmcnt(5)
	v_mfma_f32_32x32x16_bf16 v[80:95], v[230:233], v[104:107], v[80:95]
	s_waitcnt lgkmcnt(4)
	v_mfma_f32_32x32x16_bf16 v[64:79], v[234:237], v[104:107], v[64:79]
	ds_read_b128 v[230:233], v199
	ds_read_b128 v[234:237], v199 offset:4096
	ds_read_b128 v[246:249], v190
	s_waitcnt lgkmcnt(6)
	v_mfma_f32_32x32x16_bf16 v[80:95], v[238:241], v[100:103], v[80:95]
	s_waitcnt lgkmcnt(5)
	v_mfma_f32_32x32x16_bf16 v[64:79], v[242:245], v[100:103], v[64:79]
	ds_read_b128 v[238:241], v204
	ds_read_b128 v[242:245], v204 offset:4096
	ds_read_b128 v[250:253], v190 offset:1024
	v_add_u32_e32 v204, s6, v173
	s_waitcnt lgkmcnt(7)
	v_mfma_f32_32x32x16_bf16 v[80:95], v[200:203], v[96:99], v[80:95]
	s_waitcnt lgkmcnt(6)
	v_mfma_f32_32x32x16_bf16 v[64:79], v[226:229], v[96:99], v[64:79]
	ds_read_b128 v[200:203], v205
	ds_read_b128 v[226:229], v205 offset:4096
	s_waitcnt lgkmcnt(5)
	v_mfma_f32_32x32x16_bf16 v[80:95], v[230:233], v[246:249], v[80:95]
	s_waitcnt lgkmcnt(5)
	v_mfma_f32_32x32x16_bf16 v[64:79], v[234:237], v[246:249], v[64:79]
	ds_read_b128 v[230:233], v204
	ds_read_b128 v[234:237], v204 offset:4096
	ds_read_b128 v[246:249], v190 offset:2048
	s_waitcnt lgkmcnt(5)
	v_mfma_f32_32x32x16_bf16 v[80:95], v[238:241], v[250:253], v[80:95]
	s_waitcnt lgkmcnt(5)
	v_mfma_f32_32x32x16_bf16 v[64:79], v[242:245], v[250:253], v[64:79]
	ds_read_b128 v[250:253], v190 offset:3072
	s_waitcnt lgkmcnt(1)
	v_mfma_f32_32x32x16_bf16 v[80:95], v[200:203], v[246:249], v[80:95]
	v_exp_f32_e32 v205, v133
	v_cvt_pk_bf16_f32 v133, v211, v213
	v_cvt_pk_bf16_f32 v138, v165, v205
	v_add_f32_e32 v128, v205, v128
	v_add_f32_e32 v128, v206, v128
	v_add_f32_e32 v128, v215, v128
	s_waitcnt lgkmcnt(1)
	v_mfma_f32_32x32x16_bf16 v[64:79], v[226:229], v[246:249], v[64:79]
	v_add_f32_e32 v128, v216, v128
	v_add_f32_e32 v128, v225, v128
	v_add_f32_e32 v128, v162, v128
	v_add_f32_e32 v128, v163, v128
	v_add_f32_e32 v128, v160, v128
	v_add_f32_e32 v128, v161, v128
	s_waitcnt lgkmcnt(0)
	v_mfma_f32_32x32x16_bf16 v[80:95], v[230:233], v[250:253], v[80:95]
	v_exp_f32_e32 v226, v134
	v_exp_f32_e32 v227, v135
	v_cvt_pk_bf16_f32 v134, v208, v210
	v_cvt_pk_bf16_f32 v135, v207, v209
	v_add_f32_e32 v128, v226, v128
	v_add_f32_e32 v203, v227, v128
	v_mov_b32_e32 v204, v203
	s_waitcnt lgkmcnt(0)
	v_mfma_f32_32x32x16_bf16 v[64:79], v[234:237], v[250:253], v[64:79]
	s_nop 0
	v_permlane32_swap_b32_e32 v203, v204
	v_cvt_pk_bf16_f32 v128, v222, v224
	v_cvt_pk_bf16_f32 v208, v216, v225
	v_cvt_pk_bf16_f32 v209, v162, v163
	v_cvt_pk_bf16_f32 v210, v160, v161
	v_cvt_pk_bf16_f32 v211, v226, v227
	v_permlane32_swap_b32_e32 v132, v134
	v_permlane32_swap_b32_e32 v128, v130
	v_permlane32_swap_b32_e32 v133, v135
	v_permlane32_swap_b32_e32 v136, v138
	v_permlane32_swap_b32_e32 v208, v210
	v_permlane32_swap_b32_e32 v209, v211
	ds_read_b64_tr_b16 v[160:161], v167 offset:0
	ds_read_b64_tr_b16 v[162:163], v167 offset:0x800
	ds_read_b64_tr_b16 v[232:233], v167 offset:0x1000
	ds_read_b64_tr_b16 v[234:235], v167 offset:0x1800
	ds_read_b64_tr_b16 v[236:237], v167 offset:0x2000
	ds_read_b64_tr_b16 v[238:239], v167 offset:0x2800
	ds_read_b64_tr_b16 v[240:241], v167 offset:0x3000
	ds_read_b64_tr_b16 v[242:243], v167 offset:0x3800
	v_max_f32_e32 v164, v81, v81
	v_max_f32_e32 v165, v80, v80
	v_max_f32_e32 v164, v165, v164
	v_max3_f32 v164, v164, v82, v83
	v_max3_f32 v164, v164, v84, v85
	v_max3_f32 v164, v164, v86, v87
	v_max3_f32 v164, v164, v88, v89
	v_max3_f32 v164, v164, v90, v91
	v_max3_f32 v164, v164, v92, v93
	v_max3_f32 v164, v164, v94, v95
	s_waitcnt lgkmcnt(0)
	v_mfma_f32_32x32x16_bf16 v[0:15], v[128:131], v[160:163], v[0:15]
	v_max3_f32 v160, v164, v64, v65
	v_max3_f32 v160, v160, v66, v67
	v_max3_f32 v160, v160, v68, v69
	v_mfma_f32_32x32x16_bf16 v[0:15], v[132:135], v[232:235], v[0:15]
	ds_read_b64_tr_b16 v[232:233], v167 offset:0x200
	ds_read_b64_tr_b16 v[234:235], v167 offset:0xa00
	v_max3_f32 v160, v160, v70, v71
	v_max3_f32 v160, v160, v72, v73
	v_max3_f32 v160, v160, v74, v75
	v_mfma_f32_32x32x16_bf16 v[0:15], v[136:139], v[236:239], v[0:15]
	ds_read_b64_tr_b16 v[236:237], v167 offset:0x1200
	ds_read_b64_tr_b16 v[238:239], v167 offset:0x1a00
	ds_read_b64_tr_b16 v[244:245], v167 offset:0x2200
	ds_read_b64_tr_b16 v[246:247], v167 offset:0x2a00
	ds_read_b64_tr_b16 v[248:249], v167 offset:0x3200
	ds_read_b64_tr_b16 v[250:251], v167 offset:0x3a00
	v_max3_f32 v160, v160, v76, v77
	v_max3_f32 v160, v160, v78, v79
	v_mov_b32_e32 v161, v160
	v_mfma_f32_32x32x16_bf16 v[0:15], v[208:211], v[240:243], v[0:15]
	v_max_f32_e32 v162, v198, v198
	v_permlane32_swap_b32_e32 v160, v161
	v_max_f32_e32 v161, v161, v161
	v_max_f32_e32 v160, v160, v160
	v_max_f32_e32 v160, v160, v161
	s_waitcnt lgkmcnt(0)
	v_mfma_f32_32x32x16_bf16 v[32:47], v[128:131], v[232:235], v[32:47]
	ds_read_b64_tr_b16 v[232:233], v167 offset:0x400
	ds_read_b64_tr_b16 v[234:235], v167 offset:0xc00
	v_sub_f32_e32 v161, v160, v198
	v_max_f32_e32 v160, v162, v160
	v_sub_f32_e32 v162, v198, v160
	v_mul_f32_e32 v162, 0x3dd53b94, v162
	v_exp_f32_e32 v162, v162
	v_mfma_f32_32x32x16_bf16 v[32:47], v[132:135], v[236:239], v[32:47]
	ds_read_b64_tr_b16 v[236:237], v167 offset:0x1400
	ds_read_b64_tr_b16 v[238:239], v167 offset:0x1c00
	ds_read_b64_tr_b16 v[240:241], v167 offset:0x2400
	ds_read_b64_tr_b16 v[242:243], v167 offset:0x2c00
	v_cmp_ge_f32_e32 vcc, s46, v161
	s_cmp_eq_u64 vcc, exec
	s_cselect_b64 s[6:7], -1, 0
	v_cndmask_b32_e64 v206, v162, 1.0, s[6:7]
	v_cndmask_b32_e64 v160, v160, v198, s[6:7]
	v_mul_f32_e32 v205, 0xbdd53b94, v160
	v_cmp_gt_f32_e32 vcc, 1.0, v206
	v_mfma_f32_32x32x16_bf16 v[32:47], v[136:139], v[244:247], v[32:47]
	ds_read_b64_tr_b16 v[244:245], v167 offset:0x3400
	ds_read_b64_tr_b16 v[246:247], v167 offset:0x3c00
	v_fmamk_f32 v87, v87, 0x3dd53b94, v205
	v_fmamk_f32 v80, v80, 0x3dd53b94, v205
	v_fmamk_f32 v81, v81, 0x3dd53b94, v205
	v_fmamk_f32 v82, v82, 0x3dd53b94, v205
	v_fmamk_f32 v83, v83, 0x3dd53b94, v205
	v_mfma_f32_32x32x16_bf16 v[32:47], v[208:211], v[248:251], v[32:47]
	v_fmamk_f32 v84, v84, 0x3dd53b94, v205
	v_fmamk_f32 v85, v85, 0x3dd53b94, v205
	v_fmamk_f32 v86, v86, 0x3dd53b94, v205
	v_fmamk_f32 v88, v88, 0x3dd53b94, v205
	v_fmamk_f32 v89, v89, 0x3dd53b94, v205
	s_waitcnt lgkmcnt(0)
	v_mfma_f32_32x32x16_bf16 v[16:31], v[128:131], v[232:235], v[16:31]
	ds_read_b64_tr_b16 v[232:233], v167 offset:0x600
	ds_read_b64_tr_b16 v[234:235], v167 offset:0xe00
	v_fmamk_f32 v90, v90, 0x3dd53b94, v205
	v_fmamk_f32 v91, v91, 0x3dd53b94, v205
	v_fmamk_f32 v92, v92, 0x3dd53b94, v205
	v_fmamk_f32 v93, v93, 0x3dd53b94, v205
	v_fmamk_f32 v94, v94, 0x3dd53b94, v205
	v_mfma_f32_32x32x16_bf16 v[16:31], v[132:135], v[236:239], v[16:31]
	ds_read_b64_tr_b16 v[236:237], v167 offset:0x1600
	ds_read_b64_tr_b16 v[238:239], v167 offset:0x1e00
	v_fmamk_f32 v95, v95, 0x3dd53b94, v205
	v_fmamk_f32 v215, v64, 0x3dd53b94, v205
	v_fmamk_f32 v216, v65, 0x3dd53b94, v205
	v_fmamk_f32 v217, v66, 0x3dd53b94, v205
	v_fmamk_f32 v218, v67, 0x3dd53b94, v205
	v_mfma_f32_32x32x16_bf16 v[16:31], v[136:139], v[240:243], v[16:31]
	ds_read_b64_tr_b16 v[240:241], v167 offset:0x2600
	ds_read_b64_tr_b16 v[242:243], v167 offset:0x2e00
	ds_read_b64_tr_b16 v[248:249], v167 offset:0x3600
	ds_read_b64_tr_b16 v[250:251], v167 offset:0x3e00
	v_fmamk_f32 v219, v68, 0x3dd53b94, v205
	v_fmamk_f32 v212, v73, 0x3dd53b94, v205
	v_fmamk_f32 v213, v74, 0x3dd53b94, v205
	v_fmamk_f32 v214, v75, 0x3dd53b94, v205
	v_mfma_f32_32x32x16_bf16 v[16:31], v[208:211], v[244:247], v[16:31]
	v_fmamk_f32 v207, v76, 0x3dd53b94, v205
	v_fmamk_f32 v220, v77, 0x3dd53b94, v205
	v_fmamk_f32 v221, v78, 0x3dd53b94, v205
	s_waitcnt lgkmcnt(0)
	v_mfma_f32_32x32x16_bf16 v[48:63], v[128:131], v[232:235], v[48:63]
	v_exp_f32_e32 v128, v80
	v_exp_f32_e32 v129, v82
	v_exp_f32_e32 v130, v84
	v_exp_f32_e32 v131, v86
	v_mfma_f32_32x32x16_bf16 v[48:63], v[132:135], v[236:239], v[48:63]
	v_exp_f32_e32 v132, v88
	v_exp_f32_e32 v133, v90
	v_exp_f32_e32 v134, v92
	v_exp_f32_e32 v135, v94
	v_mfma_f32_32x32x16_bf16 v[48:63], v[136:139], v[240:243], v[48:63]
	v_exp_f32_e32 v139, v89
	v_exp_f32_e32 v138, v91
	v_exp_f32_e32 v137, v93
	v_exp_f32_e32 v136, v95
	v_mfma_f32_32x32x16_bf16 v[48:63], v[208:211], v[248:251], v[48:63]
	v_exp_f32_e32 v161, v87
	v_exp_f32_e32 v198, v81
	v_exp_f32_e32 v163, v83
	v_exp_f32_e32 v162, v85
	v_fmamk_f32 v208, v69, 0x3dd53b94, v205
	v_fmamk_f32 v209, v70, 0x3dd53b94, v205
	v_fmamk_f32 v210, v71, 0x3dd53b94, v205
	v_fmamk_f32 v211, v72, 0x3dd53b94, v205
	v_fmac_f32_e32 v205, 0x3dd53b94, v79
	s_cbranch_vccz .LBB0_2016
	s_and_saveexec_b64 s[10:11], s[4:5]
	ds_write_b32 v189, v206 offset:128
	s_or_b64 exec, exec, s[10:11]
	s_waitcnt lgkmcnt(0)
	v_add_u32_e32 v248, s12, v169
	ds_read_b128 v[232:235], v248 offset:224
	ds_read_b128 v[236:239], v248 offset:192
	ds_read_b128 v[240:243], v248 offset:160
	ds_read_b128 v[244:247], v248 offset:128
	s_waitcnt lgkmcnt(3)
	v_pk_mul_f32 v[12:13], v[12:13], v[232:233]
	s_waitcnt lgkmcnt(2)
	v_pk_mul_f32 v[8:9], v[8:9], v[236:237]
	s_waitcnt lgkmcnt(1)
	v_pk_mul_f32 v[4:5], v[4:5], v[240:241]
	v_pk_mul_f32 v[14:15], v[14:15], v[234:235]
	v_pk_mul_f32 v[10:11], v[10:11], v[238:239]
	v_pk_mul_f32 v[6:7], v[6:7], v[242:243]
	s_waitcnt lgkmcnt(0)
	v_pk_mul_f32 v[2:3], v[2:3], v[246:247]
	v_pk_mul_f32 v[0:1], v[0:1], v[244:245]
	v_pk_mul_f32 v[44:45], v[44:45], v[232:233]
	v_pk_mul_f32 v[40:41], v[40:41], v[236:237]
	v_pk_mul_f32 v[36:37], v[36:37], v[240:241]
	v_pk_mul_f32 v[46:47], v[46:47], v[234:235]
	v_pk_mul_f32 v[42:43], v[42:43], v[238:239]
	v_pk_mul_f32 v[38:39], v[38:39], v[242:243]
	v_pk_mul_f32 v[34:35], v[34:35], v[246:247]
	v_pk_mul_f32 v[32:33], v[32:33], v[244:245]
	v_pk_mul_f32 v[28:29], v[28:29], v[232:233]
	v_pk_mul_f32 v[24:25], v[24:25], v[236:237]
	v_pk_mul_f32 v[20:21], v[20:21], v[240:241]
	v_pk_mul_f32 v[30:31], v[30:31], v[234:235]
	v_pk_mul_f32 v[26:27], v[26:27], v[238:239]
	v_pk_mul_f32 v[22:23], v[22:23], v[242:243]
	v_pk_mul_f32 v[18:19], v[18:19], v[246:247]
	v_pk_mul_f32 v[16:17], v[16:17], v[244:245]
	v_pk_mul_f32 v[60:61], v[60:61], v[232:233]
	v_pk_mul_f32 v[56:57], v[56:57], v[236:237]
	v_pk_mul_f32 v[52:53], v[52:53], v[240:241]
	v_pk_mul_f32 v[62:63], v[62:63], v[234:235]
	v_pk_mul_f32 v[58:59], v[58:59], v[238:239]
	v_pk_mul_f32 v[54:55], v[54:55], v[242:243]
	v_pk_mul_f32 v[50:51], v[50:51], v[246:247]
	v_pk_mul_f32 v[48:49], v[48:49], v[244:245]
